# speedup vs baseline: 1.0299x; 1.0099x over previous
_ZN12_GLOBAL__N_113search_kernelEPKfS1_PhPf:
	s_load_dwordx2 s[8:9], s[0:1], 0x0
	s_load_dwordx2 s[4:5], s[0:1], 0x10
	s_movk_i32 s3, 0x90
	v_readfirstlane_b32 s10, v0
	v_cmp_gt_u32_e32 vcc, s3, v0
	s_and_saveexec_b64 s[6:7], vcc
	v_mov_b32_e32 v2, -1
	v_lshlrev_b32_e32 v1, 3, v0
	v_mov_b32_e32 v3, v2
	ds_write_b64 v1, v[2:3] offset:16384
	s_or_b64 exec, exec, s[6:7]
	s_waitcnt lgkmcnt(0)
	s_add_u32 s6, s4, 0x240000
	s_addc_u32 s7, s5, 0
	s_lshl_b32 s11, s2, 1
	s_and_b32 s14, s11, 14
	s_ashr_i32 s11, s2, 7
	s_lshr_b32 s15, s10, 6
	s_add_i32 s14, s14, s11
	s_bfe_u32 s2, s2, 0x40003
	s_mul_i32 s11, s15, 24
	v_mul_u32_u24_e32 v2, 0x71d, v0
	v_mul_u32_u24_e32 v4, 0x195, v0
	s_min_u32 s18, s11, 0xa5
	s_mul_i32 s11, s14, 3
	s_mul_i32 s12, s2, 9
	s_mov_b32 s13, 0
	v_lshrrev_b32_e32 v3, 16, v2
	s_movk_i32 s19, 0xffdc
	v_lshrrev_b32_e32 v5, 17, v4
	v_mad_i32_i24 v2, v3, s19, v0
	v_mad_i32_i24 v4, v5, -9, v3
	v_add_u32_e32 v3, s11, v5
	v_mov_b64_e32 v[6:7], s[12:13]
	v_mad_i64_i32 v[8:9], s[16:17], v3, s3, v[6:7]
	v_ashrrev_i32_e32 v5, 31, v4
	v_lshl_add_u64 v[4:5], v[8:9], 0, v[4:5]
	s_movk_i32 s13, 0x240
	v_mov_b64_e32 v[8:9], s[8:9]
	v_mad_u64_u32 v[10:11], s[8:9], v4, s13, v[8:9]
	v_min_u32_e32 v4, 0x1cb, v0
	v_or_b32_e32 v4, 0x200, v4
	v_mad_i32_i24 v11, v5, s13, v11
	v_mul_u32_u24_e32 v5, 0x71d, v4
	v_ashrrev_i32_e32 v3, 31, v2
	v_lshrrev_b32_e32 v5, 16, v5
	v_lshl_add_u64 v[2:3], v[2:3], 4, v[10:11]
	v_mad_i32_i24 v10, v5, s19, v4
	v_mul_u32_u24_e32 v4, 0x653, v4
	v_lshrrev_b32_e32 v11, 19, v4
	v_mad_i32_i24 v4, v11, -9, v5
	v_add_u32_e32 v5, s11, v11
	v_mad_i64_i32 v[6:7], s[8:9], v5, s3, v[6:7]
	v_ashrrev_i32_e32 v5, 31, v4
	v_lshl_add_u64 v[4:5], v[6:7], 0, v[4:5]
	v_mad_u64_u32 v[12:13], s[8:9], v4, s13, v[8:9]
	s_mul_i32 s8, s14, 0x90
	s_barrier
	s_load_dwordx2 s[42:43], s[0:1], 0x8
	v_mov_b32_e32 v16, 0
	v_mov_b32_e32 v17, 0
	ds_write_b64 v16, v[16:17] offset:18112
	s_load_dwordx2 s[62:63], s[0:1], 0x0
	v_mov_b32_e32 v244, v2
	v_mov_b32_e32 v245, v3
	global_load_dwordx4 v[6:9], v[2:3], off
	v_mad_i32_i24 v13, v5, s13, v13
	v_ashrrev_i32_e32 v11, 31, v10
	v_lshl_add_u64 v[10:11], v[10:11], 4, v[12:13]
	v_mov_b32_e32 v246, v10
	v_mov_b32_e32 v247, v11
	global_load_dwordx4 v[10:13], v[10:11], off
	v_and_b32_e32 v1, 63, v0
	s_add_i32 s20, s8, s12
	s_lshl_b32 s20, s20, 10
	v_lshl_add_u32 v164, v1, 4, s20
	s_mul_i32 s9, s14, 0xbd
	s_add_i32 s21, s9, s18
	s_lshl_b32 s21, s21, 10
	v_lshl_add_u32 v165, v1, 4, s21
	s_add_u32 s22, s4, 0x1000
	s_addc_u32 s23, s5, 0
	s_add_u32 s24, s4, 0x2000
	s_addc_u32 s25, s5, 0
	s_mov_b32 s26, s6
	s_mov_b32 s27, s7
	s_add_u32 s28, s6, 0x1000
	s_addc_u32 s29, s7, 0
	s_add_u32 s30, s6, 0x2000
	s_addc_u32 s31, s7, 0
	s_add_u32 s32, s6, 0x3000
	s_addc_u32 s33, s7, 0
	s_add_u32 s34, s6, 0x4000
	s_addc_u32 s35, s7, 0
	s_add_u32 s36, s6, 0x5000
	s_addc_u32 s37, s7, 0
	v_bfe_u32 v166, v0, 4, 2
	v_and_b32_e32 v167, 15, v0
	v_lshlrev_b32_e32 v167, 3, v167
	s_mul_i32 s40, s15, 6
	s_mov_b32 s41, 0x7f000000
	global_load_dwordx4 v[112:115], v164, s[4:5]
	global_load_dwordx4 v[16:19], v165, s[26:27] nt
	global_load_dwordx4 v[20:23], v165, s[26:27] offset:1024 nt
	global_load_dwordx4 v[24:27], v165, s[26:27] offset:2048 nt
	global_load_dwordx4 v[28:31], v165, s[26:27] offset:3072 nt
	global_load_dwordx4 v[32:35], v165, s[28:29] nt
	global_load_dwordx4 v[36:39], v165, s[28:29] offset:1024 nt
	global_load_dwordx4 v[40:43], v165, s[28:29] offset:2048 nt
	global_load_dwordx4 v[44:47], v165, s[28:29] offset:3072 nt
	global_load_dwordx4 v[48:51], v165, s[30:31] nt
	global_load_dwordx4 v[52:55], v165, s[30:31] offset:1024 nt
	global_load_dwordx4 v[56:59], v165, s[30:31] offset:2048 nt
	global_load_dwordx4 v[60:63], v165, s[30:31] offset:3072 nt
	global_load_dwordx4 v[64:67], v165, s[32:33] nt
	global_load_dwordx4 v[68:71], v165, s[32:33] offset:1024 nt
	global_load_dwordx4 v[72:75], v165, s[32:33] offset:2048 nt
	global_load_dwordx4 v[76:79], v165, s[32:33] offset:3072 nt
	global_load_dwordx4 v[80:83], v165, s[34:35] nt
	global_load_dwordx4 v[84:87], v165, s[34:35] offset:1024 nt
	global_load_dwordx4 v[88:91], v165, s[34:35] offset:2048 nt
	global_load_dwordx4 v[92:95], v165, s[34:35] offset:3072 nt
	global_load_dwordx4 v[96:99], v165, s[36:37] nt
	global_load_dwordx4 v[100:103], v165, s[36:37] offset:1024 nt
	global_load_dwordx4 v[104:107], v165, s[36:37] offset:2048 nt
	global_load_dwordx4 v[108:111], v165, s[36:37] offset:3072 nt
	global_load_dwordx4 v[116:119], v164, s[4:5] offset:1024
	v_lshlrev_b32_e32 v14, 4, v0
	s_lshr_b32 s50, s15, 1
	s_and_b32 s51, s15, 1
	s_lshl_b32 s51, s51, 3
	s_mov_b32 s48, 0x1010101
	s_mov_b32 s49, 0x1010101
	s_movk_i32 s58, 0x900
	s_movk_i32 s59, 0xb40
	v_and_b32_e32 v168, 7, v0
	v_lshrrev_b32_e32 v177, 3, v1
	v_or_b32_e32 v177, s51, v177
	v_lshlrev_b32_e32 v169, 3, v177
	v_and_b32_e32 v179, 3, v0
	v_lshlrev_b32_e32 v179, 8, v179
	v_lshl_add_u32 v170, v177, 4, v179
	v_add_u32_e32 v170, s20, v170
	v_lshrrev_b32_e32 v179, 2, v168
	v_and_b32_e32 v180, 3, v0
	v_lshl_or_b32 v171, v179, 4, v180
	v_mul_u32_u24_e32 v179, 11, v168
	v_lshrrev_b32_e32 v179, 5, v179
	v_mul_u32_u24_e32 v180, 3, v179
	v_sub_u32_e32 v180, v168, v180
	v_mul_u32_u24_e32 v181, 0x90, v179
	v_add_u32_e32 v181, v181, v180
	v_mul_u32_u24_e32 v172, 0x240, v181
	v_mul_u32_u24_e32 v181, 0x48, v179
	v_add_u32_e32 v181, v181, v180
	v_mul_u32_u24_e32 v173, 0x120, v181
	v_mul_u32_u24_e32 v181, 0x24, v179
	v_add_u32_e32 v181, v181, v180
	v_mul_u32_u24_e32 v174, 0x90, v181
	v_mul_u32_u24_e32 v181, 9, v179
	v_add_u32_e32 v181, v181, v180
	v_mul_u32_u24_e32 v175, 0x240, v181
	v_add_u32_e32 v176, 8, v168
	s_waitcnt lgkmcnt(0)
	s_mul_i32 s60, s14, 0x3cc00
	s_add_u32 s42, s42, s60
	s_addc_u32 s43, s43, 0
	s_mul_i32 s60, s14, 0xf300
	s_add_u32 s44, s4, s60
	s_addc_u32 s45, s5, 0
	s_add_u32 s44, s44, 0x534000
	s_addc_u32 s45, s45, 0
	s_mul_i32 s60, s14, 0x3cc0
	s_add_u32 s46, s4, s60
	s_addc_u32 s47, s5, 0
	s_add_u32 s46, s46, 0x627000
	s_addc_u32 s47, s47, 0
	v_mov_b32_e32 v152, s42
	v_mov_b32_e32 v153, s43
	v_mov_b32_e32 v154, s44
	v_mov_b32_e32 v155, s45
	v_mov_b32_e32 v159, s46
	v_mov_b32_e32 v161, s47
	s_sub_u32 s60, s42, s62
	s_subb_u32 s61, s43, s63
	s_mul_i32 s62, s14, 0x3cc00
	s_sub_u32 s60, s60, s62
	s_subb_u32 s61, s61, 0
	v_lshl_add_u64 v[244:245], v[244:245], 0, s[60:61]
	v_lshl_add_u64 v[246:247], v[246:247], 0, s[60:61]
	s_lshl_b32 s62, s15, 10
	s_add_i32 s62, s62, 0x46e0
	s_mov_b32 m0, s62
	s_mul_i32 s62, s2, 0xf30
	s_add_u32 s60, s44, s62
	s_addc_u32 s61, s45, 0
	v_lshlrev_b32_e32 v240, 4, v0
	v_mov_b32_e32 v241, 0
	v_lshl_add_u64 v[240:241], v[240:241], 0, s[60:61]
	s_mul_i32 s62, s2, 0x3cc
	s_add_u32 s60, s46, s62
	s_addc_u32 s61, s47, 0
	v_lshlrev_b32_e32 v242, 2, v0
	v_mov_b32_e32 v243, 0
	v_lshl_add_u64 v[242:243], v[242:243], 0, s[60:61]
	global_load_lds_dwordx4 v[244:245], off
	global_load_lds_dwordx4 v[246:247], off
	global_load_lds_dwordx4 v[240:241], off
	global_load_lds_dword v[242:243], off
	s_load_dwordx2 s[2:3], s[0:1], 0x18
	s_waitcnt vmcnt(25)
	ds_write_b128 v14, v[6:9]
	ds_write_b128 v14, v[10:13] offset:8192
	v_mfma_f32_16x16x32_f16 v[120:123], v[16:19], v[112:115], 0
	v_mfma_f32_16x16x32_f16 v[124:127], v[20:23], v[112:115], 0
	v_mfma_f32_16x16x32_f16 v[128:131], v[24:27], v[112:115], 0
	v_mfma_f32_16x16x32_f16 v[132:135], v[28:31], v[112:115], 0
	s_waitcnt vmcnt(21)
	v_mfma_f32_16x16x32_f16 v[136:139], v[32:35], v[112:115], 0
	v_mfma_f32_16x16x32_f16 v[140:143], v[36:39], v[112:115], 0
	v_mfma_f32_16x16x32_f16 v[144:147], v[40:43], v[112:115], 0
	v_mfma_f32_16x16x32_f16 v[148:151], v[44:47], v[112:115], 0
	v_min3_i32 v160, v120, v121, s41
	v_min3_i32 v160, v122, v123, v160
	v_min3_i32 v160, v124, v125, v160
	v_min3_i32 v160, v126, v127, v160
	v_min3_i32 v160, v128, v129, v160
	v_min3_i32 v160, v130, v131, v160
	v_min3_i32 v160, v132, v133, v160
	v_min3_i32 v157, v134, v135, v160
	v_mov_b32_e32 v6, 0
	v_mov_b32_e32 v7, 0x900
	v_mov_b32_e32 v8, 0x240
	s_waitcnt vmcnt(17)
	v_mfma_f32_16x16x32_f16 v[120:123], v[48:51], v[112:115], 0
	v_mfma_f32_16x16x32_f16 v[124:127], v[52:55], v[112:115], 0
	v_mov_b32_e32 v158, 0
	v_mfma_f32_16x16x32_f16 v[128:131], v[56:59], v[112:115], 0
	v_mfma_f32_16x16x32_f16 v[132:135], v[60:63], v[112:115], 0
	v_min3_i32 v160, v136, v137, v157
	v_min3_i32 v160, v138, v139, v160
	v_min3_i32 v160, v140, v141, v160
	v_min3_i32 v160, v142, v143, v160
	v_min3_i32 v160, v144, v145, v160
	v_min3_i32 v160, v146, v147, v160
	v_min3_i32 v160, v148, v149, v160
	v_min3_i32 v156, v150, v151, v160
	v_cmp_ge_i32_e32 vcc, v156, v157
	s_waitcnt vmcnt(13)
	v_mfma_f32_16x16x32_f16 v[136:139], v[64:67], v[112:115], 0
	v_mfma_f32_16x16x32_f16 v[140:143], v[68:71], v[112:115], 0
	v_cndmask_b32_e32 v158, 1, v158, vcc
	v_mfma_f32_16x16x32_f16 v[144:147], v[72:75], v[112:115], 0
	v_mfma_f32_16x16x32_f16 v[148:151], v[76:79], v[112:115], 0
	v_min3_i32 v160, v120, v121, v156
	v_min3_i32 v160, v122, v123, v160
	v_min3_i32 v160, v124, v125, v160
	v_min3_i32 v160, v126, v127, v160
	v_min3_i32 v160, v128, v129, v160
	v_min3_i32 v160, v130, v131, v160
	v_min3_i32 v160, v132, v133, v160
	v_min3_i32 v157, v134, v135, v160
	v_cmp_ge_i32_e32 vcc, v157, v156
	s_waitcnt vmcnt(9)
	v_mfma_f32_16x16x32_f16 v[120:123], v[80:83], v[112:115], 0
	v_mfma_f32_16x16x32_f16 v[124:127], v[84:87], v[112:115], 0
	v_cndmask_b32_e32 v158, 2, v158, vcc
	v_mfma_f32_16x16x32_f16 v[128:131], v[88:91], v[112:115], 0
	v_mfma_f32_16x16x32_f16 v[132:135], v[92:95], v[112:115], 0
	v_min3_i32 v160, v136, v137, v157
	v_min3_i32 v160, v138, v139, v160
	v_min3_i32 v160, v140, v141, v160
	v_min3_i32 v160, v142, v143, v160
	v_min3_i32 v160, v144, v145, v160
	v_min3_i32 v160, v146, v147, v160
	v_min3_i32 v160, v148, v149, v160
	v_min3_i32 v156, v150, v151, v160
	v_cmp_ge_i32_e32 vcc, v156, v157
	s_waitcnt vmcnt(5)
	v_mfma_f32_16x16x32_f16 v[136:139], v[96:99], v[112:115], 0
	v_mfma_f32_16x16x32_f16 v[140:143], v[100:103], v[112:115], 0
	v_cndmask_b32_e32 v158, 3, v158, vcc
	v_mfma_f32_16x16x32_f16 v[144:147], v[104:107], v[112:115], 0
	v_mfma_f32_16x16x32_f16 v[148:151], v[108:111], v[112:115], 0
	v_min3_i32 v160, v120, v121, v156
	v_min3_i32 v160, v122, v123, v160
	v_min3_i32 v160, v124, v125, v160
	v_min3_i32 v160, v126, v127, v160
	v_min3_i32 v160, v128, v129, v160
	v_min3_i32 v160, v130, v131, v160
	v_min3_i32 v160, v132, v133, v160
	v_min3_i32 v157, v134, v135, v160
	v_cmp_ge_i32_e32 vcc, v157, v156
	s_waitcnt vmcnt(4)
	global_load_dwordx4 v[112:115], v164, s[4:5] offset:2048
	v_mfma_f32_16x16x32_f16 v[120:123], v[16:19], v[116:119], 0
	v_mfma_f32_16x16x32_f16 v[124:127], v[20:23], v[116:119], 0
	v_cndmask_b32_e32 v158, 4, v158, vcc
	v_mfma_f32_16x16x32_f16 v[128:131], v[24:27], v[116:119], 0
	v_mfma_f32_16x16x32_f16 v[132:135], v[28:31], v[116:119], 0
	v_min3_i32 v160, v136, v137, v157
	v_min3_i32 v160, v138, v139, v160
	v_min3_i32 v160, v140, v141, v160
	v_min3_i32 v160, v142, v143, v160
	v_min3_i32 v160, v144, v145, v160
	v_min3_i32 v160, v146, v147, v160
	v_min3_i32 v160, v148, v149, v160
	v_min3_i32 v156, v150, v151, v160
	v_cmp_ge_i32_e32 vcc, v156, v157
	v_mfma_f32_16x16x32_f16 v[136:139], v[32:35], v[116:119], 0
	v_mfma_f32_16x16x32_f16 v[140:143], v[36:39], v[116:119], 0
	v_cndmask_b32_e32 v158, 5, v158, vcc
	v_add_u32_e32 v162, s40, v158
	v_lshl_or_b32 v162, v162, 2, v166
	v_mov_b32_e32 v163, v156
	ds_min_u64 v167, v[162:163] offset:16384
	v_mfma_f32_16x16x32_f16 v[144:147], v[40:43], v[116:119], 0
	v_mfma_f32_16x16x32_f16 v[148:151], v[44:47], v[116:119], 0
	v_min3_i32 v160, v120, v121, s41
	v_min3_i32 v160, v122, v123, v160
	v_min3_i32 v160, v124, v125, v160
	v_min3_i32 v160, v126, v127, v160
	v_min3_i32 v160, v128, v129, v160
	v_min3_i32 v160, v130, v131, v160
	v_min3_i32 v160, v132, v133, v160
	v_min3_i32 v157, v134, v135, v160
	v_mfma_f32_16x16x32_f16 v[120:123], v[48:51], v[116:119], 0
	v_mfma_f32_16x16x32_f16 v[124:127], v[52:55], v[116:119], 0
	v_mov_b32_e32 v158, 0
	v_mfma_f32_16x16x32_f16 v[128:131], v[56:59], v[116:119], 0
	v_mfma_f32_16x16x32_f16 v[132:135], v[60:63], v[116:119], 0
	v_min3_i32 v160, v136, v137, v157
	v_min3_i32 v160, v138, v139, v160
	v_min3_i32 v160, v140, v141, v160
	v_min3_i32 v160, v142, v143, v160
	v_min3_i32 v160, v144, v145, v160
	v_min3_i32 v160, v146, v147, v160
	v_min3_i32 v160, v148, v149, v160
	v_min3_i32 v156, v150, v151, v160
	v_cmp_ge_i32_e32 vcc, v156, v157
	v_mfma_f32_16x16x32_f16 v[136:139], v[64:67], v[116:119], 0
	v_mfma_f32_16x16x32_f16 v[140:143], v[68:71], v[116:119], 0
	v_cndmask_b32_e32 v158, 1, v158, vcc
	v_mfma_f32_16x16x32_f16 v[144:147], v[72:75], v[116:119], 0
	v_mfma_f32_16x16x32_f16 v[148:151], v[76:79], v[116:119], 0
	v_min3_i32 v160, v120, v121, v156
	v_min3_i32 v160, v122, v123, v160
	v_min3_i32 v160, v124, v125, v160
	v_min3_i32 v160, v126, v127, v160
	v_min3_i32 v160, v128, v129, v160
	v_min3_i32 v160, v130, v131, v160
	v_min3_i32 v160, v132, v133, v160
	v_min3_i32 v157, v134, v135, v160
	v_cmp_ge_i32_e32 vcc, v157, v156
	v_mfma_f32_16x16x32_f16 v[120:123], v[80:83], v[116:119], 0
	v_mfma_f32_16x16x32_f16 v[124:127], v[84:87], v[116:119], 0
	v_cndmask_b32_e32 v158, 2, v158, vcc
	v_mfma_f32_16x16x32_f16 v[128:131], v[88:91], v[116:119], 0
	v_mfma_f32_16x16x32_f16 v[132:135], v[92:95], v[116:119], 0
	v_min3_i32 v160, v136, v137, v157
	v_min3_i32 v160, v138, v139, v160
	v_min3_i32 v160, v140, v141, v160
	v_min3_i32 v160, v142, v143, v160
	v_min3_i32 v160, v144, v145, v160
	v_min3_i32 v160, v146, v147, v160
	v_min3_i32 v160, v148, v149, v160
	v_min3_i32 v156, v150, v151, v160
	v_cmp_ge_i32_e32 vcc, v156, v157
	v_mfma_f32_16x16x32_f16 v[136:139], v[96:99], v[116:119], 0
	v_mfma_f32_16x16x32_f16 v[140:143], v[100:103], v[116:119], 0
	v_cndmask_b32_e32 v158, 3, v158, vcc
	v_mfma_f32_16x16x32_f16 v[144:147], v[104:107], v[116:119], 0
	v_mfma_f32_16x16x32_f16 v[148:151], v[108:111], v[116:119], 0
	v_min3_i32 v160, v120, v121, v156
	v_min3_i32 v160, v122, v123, v160
	v_min3_i32 v160, v124, v125, v160
	v_min3_i32 v160, v126, v127, v160
	v_min3_i32 v160, v128, v129, v160
	v_min3_i32 v160, v130, v131, v160
	v_min3_i32 v160, v132, v133, v160
	v_min3_i32 v157, v134, v135, v160
	v_cmp_ge_i32_e32 vcc, v157, v156
	s_waitcnt vmcnt(0)
	global_load_dwordx4 v[116:119], v164, s[4:5] offset:3072
	v_mfma_f32_16x16x32_f16 v[120:123], v[16:19], v[112:115], 0
	v_mfma_f32_16x16x32_f16 v[124:127], v[20:23], v[112:115], 0
	v_cndmask_b32_e32 v158, 4, v158, vcc
	v_mfma_f32_16x16x32_f16 v[128:131], v[24:27], v[112:115], 0
	v_mfma_f32_16x16x32_f16 v[132:135], v[28:31], v[112:115], 0
	v_min3_i32 v160, v136, v137, v157
	v_min3_i32 v160, v138, v139, v160
	v_min3_i32 v160, v140, v141, v160
	v_min3_i32 v160, v142, v143, v160
	v_min3_i32 v160, v144, v145, v160
	v_min3_i32 v160, v146, v147, v160
	v_min3_i32 v160, v148, v149, v160
	v_min3_i32 v156, v150, v151, v160
	v_cmp_ge_i32_e32 vcc, v156, v157
	v_mfma_f32_16x16x32_f16 v[136:139], v[32:35], v[112:115], 0
	v_mfma_f32_16x16x32_f16 v[140:143], v[36:39], v[112:115], 0
	v_cndmask_b32_e32 v158, 5, v158, vcc
	v_add_u32_e32 v162, s40, v158
	v_lshl_or_b32 v162, v162, 2, v166
	v_mov_b32_e32 v163, v156
	ds_min_u64 v167, v[162:163] offset:16512
	v_mfma_f32_16x16x32_f16 v[144:147], v[40:43], v[112:115], 0
	v_mfma_f32_16x16x32_f16 v[148:151], v[44:47], v[112:115], 0
	v_min3_i32 v160, v120, v121, s41
	v_min3_i32 v160, v122, v123, v160
	v_min3_i32 v160, v124, v125, v160
	v_min3_i32 v160, v126, v127, v160
	v_min3_i32 v160, v128, v129, v160
	v_min3_i32 v160, v130, v131, v160
	v_min3_i32 v160, v132, v133, v160
	v_min3_i32 v157, v134, v135, v160
	v_mfma_f32_16x16x32_f16 v[120:123], v[48:51], v[112:115], 0
	v_mfma_f32_16x16x32_f16 v[124:127], v[52:55], v[112:115], 0
	v_mov_b32_e32 v158, 0
	v_mfma_f32_16x16x32_f16 v[128:131], v[56:59], v[112:115], 0
	v_mfma_f32_16x16x32_f16 v[132:135], v[60:63], v[112:115], 0
	v_min3_i32 v160, v136, v137, v157
	v_min3_i32 v160, v138, v139, v160
	v_min3_i32 v160, v140, v141, v160
	v_min3_i32 v160, v142, v143, v160
	v_min3_i32 v160, v144, v145, v160
	v_min3_i32 v160, v146, v147, v160
	v_min3_i32 v160, v148, v149, v160
	v_min3_i32 v156, v150, v151, v160
	v_cmp_ge_i32_e32 vcc, v156, v157
	v_mfma_f32_16x16x32_f16 v[136:139], v[64:67], v[112:115], 0
	v_mfma_f32_16x16x32_f16 v[140:143], v[68:71], v[112:115], 0
	v_cndmask_b32_e32 v158, 1, v158, vcc
	v_mfma_f32_16x16x32_f16 v[144:147], v[72:75], v[112:115], 0
	v_mfma_f32_16x16x32_f16 v[148:151], v[76:79], v[112:115], 0
	v_min3_i32 v160, v120, v121, v156
	v_min3_i32 v160, v122, v123, v160
	v_min3_i32 v160, v124, v125, v160
	v_min3_i32 v160, v126, v127, v160
	v_min3_i32 v160, v128, v129, v160
	v_min3_i32 v160, v130, v131, v160
	v_min3_i32 v160, v132, v133, v160
	v_min3_i32 v157, v134, v135, v160
	v_cmp_ge_i32_e32 vcc, v157, v156
	v_mfma_f32_16x16x32_f16 v[120:123], v[80:83], v[112:115], 0
	v_mfma_f32_16x16x32_f16 v[124:127], v[84:87], v[112:115], 0
	v_cndmask_b32_e32 v158, 2, v158, vcc
	v_mfma_f32_16x16x32_f16 v[128:131], v[88:91], v[112:115], 0
	v_mfma_f32_16x16x32_f16 v[132:135], v[92:95], v[112:115], 0
	v_min3_i32 v160, v136, v137, v157
	v_min3_i32 v160, v138, v139, v160
	v_min3_i32 v160, v140, v141, v160
	v_min3_i32 v160, v142, v143, v160
	v_min3_i32 v160, v144, v145, v160
	v_min3_i32 v160, v146, v147, v160
	v_min3_i32 v160, v148, v149, v160
	v_min3_i32 v156, v150, v151, v160
	v_cmp_ge_i32_e32 vcc, v156, v157
	v_mfma_f32_16x16x32_f16 v[136:139], v[96:99], v[112:115], 0
	v_mfma_f32_16x16x32_f16 v[140:143], v[100:103], v[112:115], 0
	v_cndmask_b32_e32 v158, 3, v158, vcc
	v_mfma_f32_16x16x32_f16 v[144:147], v[104:107], v[112:115], 0
	v_mfma_f32_16x16x32_f16 v[148:151], v[108:111], v[112:115], 0
	v_min3_i32 v160, v120, v121, v156
	v_min3_i32 v160, v122, v123, v160
	v_min3_i32 v160, v124, v125, v160
	v_min3_i32 v160, v126, v127, v160
	v_min3_i32 v160, v128, v129, v160
	v_min3_i32 v160, v130, v131, v160
	v_min3_i32 v160, v132, v133, v160
	v_min3_i32 v157, v134, v135, v160
	v_cmp_ge_i32_e32 vcc, v157, v156
	s_waitcnt vmcnt(0)
	global_load_dwordx4 v[112:115], v164, s[22:23]
	v_mfma_f32_16x16x32_f16 v[120:123], v[16:19], v[116:119], 0
	v_mfma_f32_16x16x32_f16 v[124:127], v[20:23], v[116:119], 0
	v_cndmask_b32_e32 v158, 4, v158, vcc
	v_mfma_f32_16x16x32_f16 v[128:131], v[24:27], v[116:119], 0
	v_mfma_f32_16x16x32_f16 v[132:135], v[28:31], v[116:119], 0
	v_min3_i32 v160, v136, v137, v157
	v_min3_i32 v160, v138, v139, v160
	v_min3_i32 v160, v140, v141, v160
	v_min3_i32 v160, v142, v143, v160
	v_min3_i32 v160, v144, v145, v160
	v_min3_i32 v160, v146, v147, v160
	v_min3_i32 v160, v148, v149, v160
	v_min3_i32 v156, v150, v151, v160
	v_cmp_ge_i32_e32 vcc, v156, v157
	v_mfma_f32_16x16x32_f16 v[136:139], v[32:35], v[116:119], 0
	v_mfma_f32_16x16x32_f16 v[140:143], v[36:39], v[116:119], 0
	v_cndmask_b32_e32 v158, 5, v158, vcc
	v_add_u32_e32 v162, s40, v158
	v_lshl_or_b32 v162, v162, 2, v166
	v_mov_b32_e32 v163, v156
	ds_min_u64 v167, v[162:163] offset:16640
	v_mfma_f32_16x16x32_f16 v[144:147], v[40:43], v[116:119], 0
	v_mfma_f32_16x16x32_f16 v[148:151], v[44:47], v[116:119], 0
	v_min3_i32 v160, v120, v121, s41
	v_min3_i32 v160, v122, v123, v160
	v_min3_i32 v160, v124, v125, v160
	v_min3_i32 v160, v126, v127, v160
	v_min3_i32 v160, v128, v129, v160
	v_min3_i32 v160, v130, v131, v160
	v_min3_i32 v160, v132, v133, v160
	v_min3_i32 v157, v134, v135, v160
	v_mfma_f32_16x16x32_f16 v[120:123], v[48:51], v[116:119], 0
	v_mfma_f32_16x16x32_f16 v[124:127], v[52:55], v[116:119], 0
	v_mov_b32_e32 v158, 0
	v_mfma_f32_16x16x32_f16 v[128:131], v[56:59], v[116:119], 0
	v_mfma_f32_16x16x32_f16 v[132:135], v[60:63], v[116:119], 0
	v_min3_i32 v160, v136, v137, v157
	v_min3_i32 v160, v138, v139, v160
	v_min3_i32 v160, v140, v141, v160
	v_min3_i32 v160, v142, v143, v160
	v_min3_i32 v160, v144, v145, v160
	v_min3_i32 v160, v146, v147, v160
	v_min3_i32 v160, v148, v149, v160
	v_min3_i32 v156, v150, v151, v160
	v_cmp_ge_i32_e32 vcc, v156, v157
	v_mfma_f32_16x16x32_f16 v[136:139], v[64:67], v[116:119], 0
	v_mfma_f32_16x16x32_f16 v[140:143], v[68:71], v[116:119], 0
	v_cndmask_b32_e32 v158, 1, v158, vcc
	v_mfma_f32_16x16x32_f16 v[144:147], v[72:75], v[116:119], 0
	v_mfma_f32_16x16x32_f16 v[148:151], v[76:79], v[116:119], 0
	v_min3_i32 v160, v120, v121, v156
	v_min3_i32 v160, v122, v123, v160
	v_min3_i32 v160, v124, v125, v160
	v_min3_i32 v160, v126, v127, v160
	v_min3_i32 v160, v128, v129, v160
	v_min3_i32 v160, v130, v131, v160
	v_min3_i32 v160, v132, v133, v160
	v_min3_i32 v157, v134, v135, v160
	v_cmp_ge_i32_e32 vcc, v157, v156
	v_mfma_f32_16x16x32_f16 v[120:123], v[80:83], v[116:119], 0
	v_mfma_f32_16x16x32_f16 v[124:127], v[84:87], v[116:119], 0
	v_cndmask_b32_e32 v158, 2, v158, vcc
	v_mfma_f32_16x16x32_f16 v[128:131], v[88:91], v[116:119], 0
	v_mfma_f32_16x16x32_f16 v[132:135], v[92:95], v[116:119], 0
	v_min3_i32 v160, v136, v137, v157
	v_min3_i32 v160, v138, v139, v160
	v_min3_i32 v160, v140, v141, v160
	v_min3_i32 v160, v142, v143, v160
	v_min3_i32 v160, v144, v145, v160
	v_min3_i32 v160, v146, v147, v160
	v_min3_i32 v160, v148, v149, v160
	v_min3_i32 v156, v150, v151, v160
	v_cmp_ge_i32_e32 vcc, v156, v157
	v_mfma_f32_16x16x32_f16 v[136:139], v[96:99], v[116:119], 0
	v_mfma_f32_16x16x32_f16 v[140:143], v[100:103], v[116:119], 0
	v_cndmask_b32_e32 v158, 3, v158, vcc
	v_mfma_f32_16x16x32_f16 v[144:147], v[104:107], v[116:119], 0
	v_mfma_f32_16x16x32_f16 v[148:151], v[108:111], v[116:119], 0
	v_min3_i32 v160, v120, v121, v156
	v_min3_i32 v160, v122, v123, v160
	v_min3_i32 v160, v124, v125, v160
	v_min3_i32 v160, v126, v127, v160
	v_min3_i32 v160, v128, v129, v160
	v_min3_i32 v160, v130, v131, v160
	v_min3_i32 v160, v132, v133, v160
	v_min3_i32 v157, v134, v135, v160
	v_cmp_ge_i32_e32 vcc, v157, v156
	s_waitcnt vmcnt(0)
	global_load_dwordx4 v[116:119], v164, s[22:23] offset:1024
	v_mfma_f32_16x16x32_f16 v[120:123], v[16:19], v[112:115], 0
	v_mfma_f32_16x16x32_f16 v[124:127], v[20:23], v[112:115], 0
	v_cndmask_b32_e32 v158, 4, v158, vcc
	v_mfma_f32_16x16x32_f16 v[128:131], v[24:27], v[112:115], 0
	v_mfma_f32_16x16x32_f16 v[132:135], v[28:31], v[112:115], 0
	v_min3_i32 v160, v136, v137, v157
	v_min3_i32 v160, v138, v139, v160
	v_min3_i32 v160, v140, v141, v160
	v_min3_i32 v160, v142, v143, v160
	v_min3_i32 v160, v144, v145, v160
	v_min3_i32 v160, v146, v147, v160
	v_min3_i32 v160, v148, v149, v160
	v_min3_i32 v156, v150, v151, v160
	v_cmp_ge_i32_e32 vcc, v156, v157
	v_mfma_f32_16x16x32_f16 v[136:139], v[32:35], v[112:115], 0
	v_mfma_f32_16x16x32_f16 v[140:143], v[36:39], v[112:115], 0
	v_cndmask_b32_e32 v158, 5, v158, vcc
	v_add_u32_e32 v162, s40, v158
	v_lshl_or_b32 v162, v162, 2, v166
	v_mov_b32_e32 v163, v156
	ds_min_u64 v167, v[162:163] offset:16768
	v_mfma_f32_16x16x32_f16 v[144:147], v[40:43], v[112:115], 0
	v_mfma_f32_16x16x32_f16 v[148:151], v[44:47], v[112:115], 0
	v_min3_i32 v160, v120, v121, s41
	v_min3_i32 v160, v122, v123, v160
	v_min3_i32 v160, v124, v125, v160
	v_min3_i32 v160, v126, v127, v160
	v_min3_i32 v160, v128, v129, v160
	v_min3_i32 v160, v130, v131, v160
	v_min3_i32 v160, v132, v133, v160
	v_min3_i32 v157, v134, v135, v160
	v_mfma_f32_16x16x32_f16 v[120:123], v[48:51], v[112:115], 0
	v_mfma_f32_16x16x32_f16 v[124:127], v[52:55], v[112:115], 0
	v_mov_b32_e32 v158, 0
	v_mfma_f32_16x16x32_f16 v[128:131], v[56:59], v[112:115], 0
	v_mfma_f32_16x16x32_f16 v[132:135], v[60:63], v[112:115], 0
	v_min3_i32 v160, v136, v137, v157
	v_min3_i32 v160, v138, v139, v160
	v_min3_i32 v160, v140, v141, v160
	v_min3_i32 v160, v142, v143, v160
	v_min3_i32 v160, v144, v145, v160
	v_min3_i32 v160, v146, v147, v160
	v_min3_i32 v160, v148, v149, v160
	v_min3_i32 v156, v150, v151, v160
	v_cmp_ge_i32_e32 vcc, v156, v157
	v_mfma_f32_16x16x32_f16 v[136:139], v[64:67], v[112:115], 0
	v_mfma_f32_16x16x32_f16 v[140:143], v[68:71], v[112:115], 0
	v_cndmask_b32_e32 v158, 1, v158, vcc
	v_mfma_f32_16x16x32_f16 v[144:147], v[72:75], v[112:115], 0
	v_mfma_f32_16x16x32_f16 v[148:151], v[76:79], v[112:115], 0
	v_min3_i32 v160, v120, v121, v156
	v_min3_i32 v160, v122, v123, v160
	v_min3_i32 v160, v124, v125, v160
	v_min3_i32 v160, v126, v127, v160
	v_min3_i32 v160, v128, v129, v160
	v_min3_i32 v160, v130, v131, v160
	v_min3_i32 v160, v132, v133, v160
	v_min3_i32 v157, v134, v135, v160
	v_cmp_ge_i32_e32 vcc, v157, v156
	v_mfma_f32_16x16x32_f16 v[120:123], v[80:83], v[112:115], 0
	v_mfma_f32_16x16x32_f16 v[124:127], v[84:87], v[112:115], 0
	v_cndmask_b32_e32 v158, 2, v158, vcc
	v_mfma_f32_16x16x32_f16 v[128:131], v[88:91], v[112:115], 0
	v_mfma_f32_16x16x32_f16 v[132:135], v[92:95], v[112:115], 0
	v_min3_i32 v160, v136, v137, v157
	v_min3_i32 v160, v138, v139, v160
	v_min3_i32 v160, v140, v141, v160
	v_min3_i32 v160, v142, v143, v160
	v_min3_i32 v160, v144, v145, v160
	v_min3_i32 v160, v146, v147, v160
	v_min3_i32 v160, v148, v149, v160
	v_min3_i32 v156, v150, v151, v160
	v_cmp_ge_i32_e32 vcc, v156, v157
	v_mfma_f32_16x16x32_f16 v[136:139], v[96:99], v[112:115], 0
	v_mfma_f32_16x16x32_f16 v[140:143], v[100:103], v[112:115], 0
	v_cndmask_b32_e32 v158, 3, v158, vcc
	v_mfma_f32_16x16x32_f16 v[144:147], v[104:107], v[112:115], 0
	v_mfma_f32_16x16x32_f16 v[148:151], v[108:111], v[112:115], 0
	v_min3_i32 v160, v120, v121, v156
	v_min3_i32 v160, v122, v123, v160
	v_min3_i32 v160, v124, v125, v160
	v_min3_i32 v160, v126, v127, v160
	v_min3_i32 v160, v128, v129, v160
	v_min3_i32 v160, v130, v131, v160
	v_min3_i32 v160, v132, v133, v160
	v_min3_i32 v157, v134, v135, v160
	v_cmp_ge_i32_e32 vcc, v157, v156
	s_waitcnt vmcnt(0)
	global_load_dwordx4 v[112:115], v164, s[22:23] offset:2048
	v_mfma_f32_16x16x32_f16 v[120:123], v[16:19], v[116:119], 0
	v_mfma_f32_16x16x32_f16 v[124:127], v[20:23], v[116:119], 0
	v_cndmask_b32_e32 v158, 4, v158, vcc
	v_mfma_f32_16x16x32_f16 v[128:131], v[24:27], v[116:119], 0
	v_mfma_f32_16x16x32_f16 v[132:135], v[28:31], v[116:119], 0
	v_min3_i32 v160, v136, v137, v157
	v_min3_i32 v160, v138, v139, v160
	v_min3_i32 v160, v140, v141, v160
	v_min3_i32 v160, v142, v143, v160
	v_min3_i32 v160, v144, v145, v160
	v_min3_i32 v160, v146, v147, v160
	v_min3_i32 v160, v148, v149, v160
	v_min3_i32 v156, v150, v151, v160
	v_cmp_ge_i32_e32 vcc, v156, v157
	v_mfma_f32_16x16x32_f16 v[136:139], v[32:35], v[116:119], 0
	v_mfma_f32_16x16x32_f16 v[140:143], v[36:39], v[116:119], 0
	v_cndmask_b32_e32 v158, 5, v158, vcc
	v_add_u32_e32 v162, s40, v158
	v_lshl_or_b32 v162, v162, 2, v166
	v_mov_b32_e32 v163, v156
	ds_min_u64 v167, v[162:163] offset:16896
	v_mfma_f32_16x16x32_f16 v[144:147], v[40:43], v[116:119], 0
	v_mfma_f32_16x16x32_f16 v[148:151], v[44:47], v[116:119], 0
	v_min3_i32 v160, v120, v121, s41
	v_min3_i32 v160, v122, v123, v160
	v_min3_i32 v160, v124, v125, v160
	v_min3_i32 v160, v126, v127, v160
	v_min3_i32 v160, v128, v129, v160
	v_min3_i32 v160, v130, v131, v160
	v_min3_i32 v160, v132, v133, v160
	v_min3_i32 v157, v134, v135, v160
	v_mfma_f32_16x16x32_f16 v[120:123], v[48:51], v[116:119], 0
	v_mfma_f32_16x16x32_f16 v[124:127], v[52:55], v[116:119], 0
	v_mov_b32_e32 v158, 0
	v_mfma_f32_16x16x32_f16 v[128:131], v[56:59], v[116:119], 0
	v_mfma_f32_16x16x32_f16 v[132:135], v[60:63], v[116:119], 0
	v_min3_i32 v160, v136, v137, v157
	v_min3_i32 v160, v138, v139, v160
	v_min3_i32 v160, v140, v141, v160
	v_min3_i32 v160, v142, v143, v160
	v_min3_i32 v160, v144, v145, v160
	v_min3_i32 v160, v146, v147, v160
	v_min3_i32 v160, v148, v149, v160
	v_min3_i32 v156, v150, v151, v160
	v_cmp_ge_i32_e32 vcc, v156, v157
	v_mfma_f32_16x16x32_f16 v[136:139], v[64:67], v[116:119], 0
	v_mfma_f32_16x16x32_f16 v[140:143], v[68:71], v[116:119], 0
	v_cndmask_b32_e32 v158, 1, v158, vcc
	v_mfma_f32_16x16x32_f16 v[144:147], v[72:75], v[116:119], 0
	v_mfma_f32_16x16x32_f16 v[148:151], v[76:79], v[116:119], 0
	v_min3_i32 v160, v120, v121, v156
	v_min3_i32 v160, v122, v123, v160
	v_min3_i32 v160, v124, v125, v160
	v_min3_i32 v160, v126, v127, v160
	v_min3_i32 v160, v128, v129, v160
	v_min3_i32 v160, v130, v131, v160
	v_min3_i32 v160, v132, v133, v160
	v_min3_i32 v157, v134, v135, v160
	v_cmp_ge_i32_e32 vcc, v157, v156
	v_mfma_f32_16x16x32_f16 v[120:123], v[80:83], v[116:119], 0
	v_mfma_f32_16x16x32_f16 v[124:127], v[84:87], v[116:119], 0
	v_cndmask_b32_e32 v158, 2, v158, vcc
	v_mfma_f32_16x16x32_f16 v[128:131], v[88:91], v[116:119], 0
	v_mfma_f32_16x16x32_f16 v[132:135], v[92:95], v[116:119], 0
	v_min3_i32 v160, v136, v137, v157
	v_min3_i32 v160, v138, v139, v160
	v_min3_i32 v160, v140, v141, v160
	v_min3_i32 v160, v142, v143, v160
	v_min3_i32 v160, v144, v145, v160
	v_min3_i32 v160, v146, v147, v160
	v_min3_i32 v160, v148, v149, v160
	v_min3_i32 v156, v150, v151, v160
	v_cmp_ge_i32_e32 vcc, v156, v157
	v_mfma_f32_16x16x32_f16 v[136:139], v[96:99], v[116:119], 0
	v_mfma_f32_16x16x32_f16 v[140:143], v[100:103], v[116:119], 0
	v_cndmask_b32_e32 v158, 3, v158, vcc
	v_mfma_f32_16x16x32_f16 v[144:147], v[104:107], v[116:119], 0
	v_mfma_f32_16x16x32_f16 v[148:151], v[108:111], v[116:119], 0
	v_min3_i32 v160, v120, v121, v156
	v_min3_i32 v160, v122, v123, v160
	v_min3_i32 v160, v124, v125, v160
	v_min3_i32 v160, v126, v127, v160
	v_min3_i32 v160, v128, v129, v160
	v_min3_i32 v160, v130, v131, v160
	v_min3_i32 v160, v132, v133, v160
	v_min3_i32 v157, v134, v135, v160
	v_cmp_ge_i32_e32 vcc, v157, v156
	s_waitcnt vmcnt(0)
	global_load_dwordx4 v[116:119], v164, s[22:23] offset:3072
	v_mfma_f32_16x16x32_f16 v[120:123], v[16:19], v[112:115], 0
	v_mfma_f32_16x16x32_f16 v[124:127], v[20:23], v[112:115], 0
	v_cndmask_b32_e32 v158, 4, v158, vcc
	v_mfma_f32_16x16x32_f16 v[128:131], v[24:27], v[112:115], 0
	v_mfma_f32_16x16x32_f16 v[132:135], v[28:31], v[112:115], 0
	v_min3_i32 v160, v136, v137, v157
	v_min3_i32 v160, v138, v139, v160
	v_min3_i32 v160, v140, v141, v160
	v_min3_i32 v160, v142, v143, v160
	v_min3_i32 v160, v144, v145, v160
	v_min3_i32 v160, v146, v147, v160
	v_min3_i32 v160, v148, v149, v160
	v_min3_i32 v156, v150, v151, v160
	v_cmp_ge_i32_e32 vcc, v156, v157
	v_mfma_f32_16x16x32_f16 v[136:139], v[32:35], v[112:115], 0
	v_mfma_f32_16x16x32_f16 v[140:143], v[36:39], v[112:115], 0
	v_cndmask_b32_e32 v158, 5, v158, vcc
	v_add_u32_e32 v162, s40, v158
	v_lshl_or_b32 v162, v162, 2, v166
	v_mov_b32_e32 v163, v156
	ds_min_u64 v167, v[162:163] offset:17024
	v_mfma_f32_16x16x32_f16 v[144:147], v[40:43], v[112:115], 0
	v_mfma_f32_16x16x32_f16 v[148:151], v[44:47], v[112:115], 0
	v_min3_i32 v160, v120, v121, s41
	v_min3_i32 v160, v122, v123, v160
	v_min3_i32 v160, v124, v125, v160
	v_min3_i32 v160, v126, v127, v160
	v_min3_i32 v160, v128, v129, v160
	v_min3_i32 v160, v130, v131, v160
	v_min3_i32 v160, v132, v133, v160
	v_min3_i32 v157, v134, v135, v160
	s_waitcnt lgkmcnt(0)
	s_barrier
	s_lshl_b32 s60, s50, 7
	v_add_u32_e32 v2, s60, v169
	ds_read_b32 v178, v2 offset:16384
	s_lshl_b32 s60, s50, 10
	v_add_u32_e32 v210, s60, v170
	s_cmp_lt_u32 s50, 2
	s_cbranch_scc0 .Lp1a_y
	s_add_i32 s65, s50, 4
	s_lshl_b32 s60, s65, 7
	v_add_u32_e32 v2, s60, v169
	ds_read_b32 v216, v2 offset:16384
	s_lshl_b32 s60, s65, 10
	v_add_u32_e32 v248, s60, v170

.Lq6:
	s_nop 1
	v_add_f32_dpp v6, v6, v6 quad_perm:[1,0,3,2] row_mask:0xf bank_mask:0xf
	s_nop 1
	v_add_f32_dpp v6, v6, v6 quad_perm:[2,3,0,1] row_mask:0xf bank_mask:0xf
	s_nop 1
	v_add_f32_dpp v6, v6, v6 row_half_mirror row_mask:0xf bank_mask:0xf
	s_nop 1
	v_add_f32_dpp v6, v6, v6 row_mirror row_mask:0xf bank_mask:0xf
	s_nop 1
	v_add_f32_dpp v6, v6, v6 row_bcast:15 row_mask:0xa bank_mask:0xf
	s_nop 1
	v_add_f32_dpp v6, v6, v6 row_bcast:31 row_mask:0xc bank_mask:0xf
	s_mov_b32 exec_lo, 0
	s_mov_b32 exec_hi, 0x80000000
	v_mul_f32_e32 v2, 0x49800000, v6
	v_rndne_f32_e32 v2, v2
	v_cvt_u32_f32_e32 v2, v2
	v_mov_b32_e32 v3, 0x1000000
	v_mov_b32_e32 v4, 0
	ds_add_rtn_u64 v[10:11], v4, v[2:3] offset:18112
	s_waitcnt lgkmcnt(0)
	v_readlane_b32 s60, v11, 63
	s_nop 3
	s_lshr_b32 s60, s60, 24
	s_cmp_eq_u32 s60, 7
	s_cbranch_scc0 .LBB1_34
	v_add_u32_e32 v2, v10, v2
	v_mov_b32_e32 v0, 0
	s_mov_b64 s[6:7], exec
	v_mbcnt_lo_u32_b32 v1, s6, 0
	v_mbcnt_hi_u32_b32 v1, s7, v1
	v_cmp_eq_u32_e32 vcc, 0, v1
	s_and_saveexec_b64 s[0:1], vcc
	s_cbranch_execz .LBB1_27
	s_lshl_b32 s8, s14, 4
	s_ashr_i32 s9, s8, 31
	s_lshl_b64 s[8:9], s[8:9], 3
	s_add_u32 s8, s4, s8
	s_addc_u32 s9, s5, s9
	s_bcnt1_i32_b64 s6, s[6:7]
	v_mov_b32_e32 v3, 0x1000000
	v_mul_lo_u32 v3, v3, s6
	v_mul_hi_u32 v4, v2, s6
	v_add_u32_e32 v5, v4, v3
	v_mul_lo_u32 v4, v2, s6
	v_mov_b32_e32 v3, 0x663000
	global_atomic_add_x2 v[4:5], v3, v[4:5], s[8:9] offset:3072 sc0
